# v60 + cleanup stack: already-satisfied lgkmcnt waits and mid-segment setprio pairs removed, m0 save/restore dropped around LDS-DMA blocks
# speedup vs baseline: 1.0042x; 1.0009x over previous
; #define PG8_STAGEB(bufoff, gbase) PG8_STAGE2(bufoff, gbase, voffB[0], voffB[1])
; #define PG8_BAR __builtin_amdgcn_s_barrier()
;     ...
;     PG8_STAGEB(PG8_SB(0, 0), cB); PG8_STAGEB(PG8_SB(0, 1), cB + hstepB); PG8_STAGEA(PG8_SA(0, 0), cA, 0); if constexpr (!HM) PG8_STAGEA(PG8_SA(0, 1), cA, 1);
;     if (wr == 1) PG8_BAR;
;     if constexpr (HM) PG8_WAIT_V(0); else PG8_WAIT_V(2);
;     PG8_BAR;
;     PG8_STAGEB(PG8_SB(1, 0), cB + kstep); PG8_STAGEA(PG8_SA(1, 0), cA + kstep, 0); PG8_STAGEB(PG8_SB(1, 1), cB + hstepB + kstep);
;     PG8_WAIT_V(6); PG8_BAR;
;     __device__ __forceinline__ void operator()(const AccT& acc, const pg8::Unit& u, int wr, int wc, int fr, int fq) const {
;         const int row0 = u.pm * 256 + wr * 64 + fr; const int pn = u.pn;
;         if (pn < 8) {
;             bf16_t* dst = (bf16_t*)(ws + (pn < 4 ? WS_U : WS_V)); const int col0 = (pn & 3) * 256 + wc * 32 + 8 * fq;
;             float* vstat = (float*)(ws + WS_VSTAT);
; #pragma unroll
;             for (int ai = 0; ai < 2; ++ai)
; #pragma unroll
;                 for (int m = 0; m < 4; ++m) { const int row = row0 + ai * 128 + m * 16; float s = 0.f, q = 0.f;
; #pragma unroll
;                     for (int bj = 0; bj < 2; ++bj) { const f32x4 v0 = gelu4(acc[ai][bj][m][0]), v1 = gelu4(acc[ai][bj][m][1]);
;                         s += (v0[0] + v0[1]) + (v0[2] + v0[3]) + (v1[0] + v1[1]) + (v1[2] + v1[3]);
;                         q += (v0[0] * v0[0] + v0[1] * v0[1]) + (v0[2] * v0[2] + v0[3] * v0[3]) + (v1[0] * v1[0] + v1[1] * v1[1]) + (v1[2] * v1[2] + v1[3] * v1[3]);
;                         u32x4 w; w.x = cvt_pk_bf16(v0[0], v0[1]); w.y = cvt_pk_bf16(v0[2], v0[3]); w.z = cvt_pk_bf16(v1[0], v1[1]); w.w = cvt_pk_bf16(v1[2], v1[3]);
;                         *(u32x4*)(dst + (size_t)row * GW + col0 + bj * 128) = w; }
;                     if (pn >= 4) { s += __shfl_xor(s, 16); s += __shfl_xor(s, 32); q += __shfl_xor(q, 16); q += __shfl_xor(q, 32);
;                         if (fq == 0) *(f32x2*)(vstat + (size_t)row * 32 + ((pn - 4) * 4 + wc) * 2) = (f32x2){s, q}; } }
;         } else if (pn < 16) {
;             bf16_t* dst = (bf16_t*)(ws + (pn < 12 ? WS_Q : WS_K)); const float sc = pn < 12 ? 1.0f : 0.08838834764831845f;
;             const float* rc = (const float*)(ws + WS_ROPEC); const float* rs = (const float*)(ws + WS_ROPES);
;             const int dd = 16 * wc + 4 * fq;
; #pragma unroll
.LBB0_132:
	v_bfe_u32 v6, v2, 4, 2
	v_and_b32_e32 v3, 15, v2
	v_lshlrev_b32_e32 v4, 4, v6
	v_lshlrev_b32_e32 v2, 2, v2
	s_and_b32 s8, s6, 3
	v_lshl_or_b32 v161, s0, 6, v3
	v_lshl_or_b32 v3, v3, 6, v4
	s_lshl_b32 s0, s0, 13
	v_and_b32_e32 v2, 32, v2
	v_bitop3_b32 v8, v3, s0, v2 bitop3:0xde
	s_lshl_b32 s0, s8, 12
	s_add_u32 s62, s94, 0x50600000
	s_addc_u32 s63, s95, 0
	s_ashr_i32 s64, s3, 31
	s_ashr_i32 s65, s92, 31
	v_bitop3_b32 v3, v3, s0, v2 bitop3:0xde
	s_add_u32 s0, s54, 0x80
	s_waitcnt vmcnt(2)
	s_barrier
	s_addc_u32 s1, s55, 0
	s_add_i32 s66, s29, 0x18000
	s_mov_b32 m0, s66
	s_nop 0
	global_load_lds_dwordx4 v1, s[0:1]
	s_add_i32 s67, s29, 0x1a000
	s_mov_b32 m0, s67
	s_nop 0
	global_load_lds_dwordx4 v156, s[0:1]
	s_add_u32 s0, s12, 0x80
	s_addc_u32 s1, s13, 0
	s_add_i32 s68, s29, 0x8000
	s_mov_b32 m0, s68
	s_nop 0
	global_load_lds_dwordx4 v157, s[0:1]
	s_add_i32 s69, s29, 0xa000
	s_mov_b32 m0, s69
	s_nop 0
	global_load_lds_dwordx4 v158, s[0:1]
	s_add_u32 s0, s54, 0x80080
	v_lshlrev_b32_e32 v2, 2, v6
	s_addc_u32 s1, s55, 0
	s_add_i32 s70, s29, 0x1c000
	s_mov_b32 m0, s70
	s_nop 0
	global_load_lds_dwordx4 v1, s[0:1]
	v_lshl_or_b32 v2, s8, 4, v2
	s_add_i32 s71, s29, 0x1e000
	s_mov_b32 m0, s71
	s_nop 0
	global_load_lds_dwordx4 v156, s[0:1]
	s_add_i32 s72, s29, 0xc000
	s_add_i32 s73, s29, 0xe000
	v_mov_b32_e32 v131, 0
	v_lshlrev_b32_e32 v130, 2, v2
	s_waitcnt vmcnt(6)
	s_cmpk_lt_u32 s4, 0x100
	v_lshl_add_u64 v[4:5], s[94:95], 0, v[130:131]
	s_mov_b64 s[0:1], 0x50800000
	v_lshlrev_b32_e32 v7, 3, v6
	s_cselect_b64 s[20:21], -1, 0
	v_lshl_add_u64 v[132:133], v[4:5], 0, s[0:1]
	s_mov_b64 s[0:1], 0x50c00000
	s_lshl_b32 s74, s8, 1
	v_add_u32_e32 v3, 0, v3
	v_lshlrev_b32_e32 v140, 1, v2
	v_mbcnt_lo_u32_b32 v2, -1, 0
	v_lshl_add_u64 v[134:135], v[4:5], 0, s[0:1]
	v_cmp_eq_u32_e64 s[6:7], 0, v6
	s_orn2_b32 s74, s74, 31
	v_lshl_or_b32 v162, s8, 5, v7
	v_mov_b32_e32 v136, s99
	v_mov_b32_e32 v137, 0
	s_add_i32 s100, s99, -1
	v_mov_b32_e32 v138, s100
	v_mov_b32_e32 v139, 0
	s_movk_i32 s75, 0x181
	v_add_u32_e32 v163, 0x10000, v3
	v_add_u32_e32 v164, 0x14000, v3
	v_add_u32_e32 v165, 0, v8
	v_add_u32_e32 v166, 0x18000, v3
	v_add_u32_e32 v167, 0x1c000, v3
	s_mov_b32 s76, 0x48600000
	s_mov_b64 s[22:23], 0x90000
	s_mov_b64 s[24:25], 0xa0000
	s_mov_b64 s[26:27], 0xb0000
	s_mov_b32 s77, 0x3c600000
	s_mov_b32 s78, 0x38600000
	s_mov_b32 s28, 0x3e6d3388
	s_mov_b32 s30, 0x3f07dc22
	s_mov_b32 s34, 0xbf3a00e3
	s_mov_b32 s36, 0x3f35f0e3
	s_mov_b32 s38, 0xbe11a98e
	s_mov_b32 s40, 0x3e027906
	s_mov_b32 s42, 0xbf38aa3b
	v_mov_b32_e32 v168, 0x3db504f3
	v_mbcnt_hi_u32_b32 v169, -1, v2
	s_mov_b32 s79, 0
	s_barrier
	s_branch .LBB0_135
